# moe_setup index fill unrolled with reads in flight; prologue silu table loads issued together
# baseline (speedup 1.0000x reference)
.LBB0_7:
	s_load_dwordx16 s[16:31], s[0:1], 0x0
	s_lshl_b32 s52, s2, 5
	s_and_b32 s3, s52, 0xe0
	s_bfe_u32 s4, s2, 0x50003
	s_waitcnt lgkmcnt(0)
	v_writelane_b32 v251, s16, 3
	s_nop 1
	v_writelane_b32 v251, s17, 4
	v_writelane_b32 v251, s18, 5
	v_writelane_b32 v251, s19, 6
	v_writelane_b32 v251, s20, 7
	v_writelane_b32 v251, s21, 8
	v_writelane_b32 v251, s22, 9
	v_writelane_b32 v251, s23, 10
	v_writelane_b32 v251, s24, 11
	v_writelane_b32 v251, s25, 12
	v_writelane_b32 v251, s26, 13
	v_writelane_b32 v251, s27, 14
	v_writelane_b32 v251, s28, 15
	v_writelane_b32 v251, s29, 16
	v_writelane_b32 v251, s30, 17
	v_writelane_b32 v251, s31, 18
	s_load_dwordx16 s[16:31], s[0:1], 0x40
	s_waitcnt lgkmcnt(0)
	v_writelane_b32 v251, s16, 19
	s_nop 1
	v_writelane_b32 v251, s17, 20
	v_writelane_b32 v251, s18, 21
	v_writelane_b32 v251, s19, 22
	v_writelane_b32 v251, s20, 23
	v_writelane_b32 v251, s21, 24
	v_writelane_b32 v251, s22, 25
	v_writelane_b32 v251, s23, 26
	v_writelane_b32 v251, s24, 27
	v_writelane_b32 v251, s25, 28
	v_writelane_b32 v251, s26, 29
	v_writelane_b32 v251, s27, 30
	v_writelane_b32 v251, s28, 31
	v_writelane_b32 v251, s29, 32
	v_writelane_b32 v251, s30, 33
	v_writelane_b32 v251, s31, 34
	s_load_dwordx16 s[16:31], s[0:1], 0x80
	s_waitcnt lgkmcnt(0)
	v_writelane_b32 v251, s16, 35
	s_nop 1
	v_writelane_b32 v251, s17, 36
	v_writelane_b32 v251, s18, 37
	v_writelane_b32 v251, s19, 38
	v_writelane_b32 v251, s20, 39
	v_writelane_b32 v251, s21, 40
	v_writelane_b32 v251, s22, 41
	v_writelane_b32 v251, s23, 42
	v_writelane_b32 v251, s24, 43
	v_writelane_b32 v251, s25, 44
	v_writelane_b32 v251, s26, 45
	v_writelane_b32 v251, s27, 46
	v_writelane_b32 v251, s28, 47
	v_writelane_b32 v251, s29, 48
	v_writelane_b32 v251, s30, 49
	v_writelane_b32 v251, s31, 50
	s_load_dwordx16 s[16:31], s[0:1], 0xc0
	v_writelane_b32 v251, s4, 51
	s_or_b32 s4, s3, s4
	v_writelane_b32 v251, s4, 52
	s_lshl_b32 s4, s4, 3
	v_writelane_b32 v251, s4, 53
	s_load_dwordx2 s[4:5], s[0:1], 0x110
	s_waitcnt lgkmcnt(0)
	v_writelane_b32 v251, s16, 54
	s_cmp_lt_i32 s4, 1
	s_nop 0
	v_writelane_b32 v251, s17, 55
	v_writelane_b32 v251, s18, 56
	v_writelane_b32 v251, s19, 57
	v_writelane_b32 v251, s20, 58
	v_writelane_b32 v252, s26, 0
	v_writelane_b32 v251, s21, 59
	v_writelane_b32 v252, s27, 1
	s_cselect_b64 s[14:15], -1, 0
	s_cmp_gt_i32 s5, 0
	v_writelane_b32 v251, s22, 60
	v_writelane_b32 v252, s28, 2
	s_cselect_b64 s[4:5], -1, 0
	v_writelane_b32 v251, s23, 61
	v_writelane_b32 v252, s29, 3
	v_writelane_b32 v251, s24, 62
	v_writelane_b32 v252, s30, 4
	s_and_b64 s[4:5], s[14:15], s[4:5]
	v_writelane_b32 v251, s25, 63
	v_writelane_b32 v252, s31, 5
	s_andn2_b64 vcc, exec, s[4:5]
	s_cbranch_vccnz .LBB0_1136
	v_mov_b32_e32 v68, v0
	s_movk_i32 s4, 0x1400
	s_mov_b32 s20, 0
	s_nop 0
	v_readfirstlane_b32 s18, v68
	v_cmp_gt_i32_e32 vcc, s4, v68
	s_and_saveexec_b64 s[4:5], vcc
	s_load_dwordx16 s[36:51], s[0:1], 0x0
	s_cbranch_execz .LBB0_11
	s_waitcnt lgkmcnt(0)
	v_mov_b32_e32 v2, s38
	v_mov_b32_e32 v3, s39
	v_ashrrev_i32_e32 v69, 31, v68
	v_lshl_add_u32 v1, v68, 2, 0
	v_lshl_add_u64 v[2:3], v[68:69], 2, v[2:3]
	v_add_u32_e32 v1, 0x12000, v1
	v_lshl_add_u64 v[4:5], v[68:69], 2, s[42:43]
	s_mov_b64 s[6:7], 0x1000
	s_mov_b64 s[8:9], 0x2000
	s_mov_b64 s[10:11], 0x3000
	v_lshl_add_u64 v[6:7], v[2:3], 0, s[6:7]
	v_lshl_add_u64 v[8:9], v[2:3], 0, s[8:9]
	v_lshl_add_u64 v[10:11], v[2:3], 0, s[10:11]
	global_load_dword v100, v[2:3], off
	global_load_dword v101, v[2:3], off offset:2048
	global_load_dword v102, v[6:7], off
	global_load_dword v103, v[6:7], off offset:2048
	global_load_dword v104, v[8:9], off
	global_load_dword v105, v[8:9], off offset:2048
	global_load_dword v106, v[10:11], off
	global_load_dword v107, v[10:11], off offset:2048
	global_load_dword v108, v[4:5], off
	global_load_dword v109, v[4:5], off offset:2048
	s_waitcnt vmcnt(0)
	v_mul_f32_e32 v112, 0xbfb8aa3b, v100
	v_exp_f32_e32 v112, v112
	s_nop 0
	v_add_f32_e32 v112, 1.0, v112
	v_rcp_f32_e32 v112, v112
	s_nop 0
	v_mul_f32_e32 v100, v100, v112
	ds_write_b32 v1, v100
	v_mul_f32_e32 v113, 0xbfb8aa3b, v101
	v_exp_f32_e32 v113, v113
	s_nop 0
	v_add_f32_e32 v113, 1.0, v113
	v_rcp_f32_e32 v113, v113
	s_nop 0
	v_mul_f32_e32 v101, v101, v113
	ds_write_b32 v1, v101 offset:2048
	v_mul_f32_e32 v112, 0xbfb8aa3b, v102
	v_exp_f32_e32 v112, v112
	s_nop 0
	v_add_f32_e32 v112, 1.0, v112
	v_rcp_f32_e32 v112, v112
	s_nop 0
	v_mul_f32_e32 v102, v102, v112
	ds_write_b32 v1, v102 offset:4096
	v_mul_f32_e32 v113, 0xbfb8aa3b, v103
	v_exp_f32_e32 v113, v113
	s_nop 0
	v_add_f32_e32 v113, 1.0, v113
	v_rcp_f32_e32 v113, v113
	s_nop 0
	v_mul_f32_e32 v103, v103, v113
	ds_write_b32 v1, v103 offset:6144
	v_mul_f32_e32 v112, 0xbfb8aa3b, v104
	v_exp_f32_e32 v112, v112
	s_nop 0
	v_add_f32_e32 v112, 1.0, v112
	v_rcp_f32_e32 v112, v112
	s_nop 0
	v_mul_f32_e32 v104, v104, v112
	ds_write_b32 v1, v104 offset:8192
	v_mul_f32_e32 v113, 0xbfb8aa3b, v105
	v_exp_f32_e32 v113, v113
	s_nop 0
	v_add_f32_e32 v113, 1.0, v113
	v_rcp_f32_e32 v113, v113
	s_nop 0
	v_mul_f32_e32 v105, v105, v113
	ds_write_b32 v1, v105 offset:10240
	v_mul_f32_e32 v112, 0xbfb8aa3b, v106
	v_exp_f32_e32 v112, v112
	s_nop 0
	v_add_f32_e32 v112, 1.0, v112
	v_rcp_f32_e32 v112, v112
	s_nop 0
	v_mul_f32_e32 v106, v106, v112
	ds_write_b32 v1, v106 offset:12288
	v_mul_f32_e32 v113, 0xbfb8aa3b, v107
	v_exp_f32_e32 v113, v113
	s_nop 0
	v_add_f32_e32 v113, 1.0, v113
	v_rcp_f32_e32 v113, v113
	s_nop 0
	v_mul_f32_e32 v107, v107, v113
	ds_write_b32 v1, v107 offset:14336
	v_mul_f32_e32 v112, 0xbfb8aa3b, v108
	v_exp_f32_e32 v112, v112
	s_nop 0
	v_add_f32_e32 v112, 1.0, v112
	v_rcp_f32_e32 v112, v112
	s_nop 0
	v_mul_f32_e32 v108, v108, v112
	ds_write_b32 v1, v108 offset:16384
	v_mul_f32_e32 v113, 0xbfb8aa3b, v109
	v_exp_f32_e32 v113, v113
	s_nop 0
	v_add_f32_e32 v113, 1.0, v113
	v_rcp_f32_e32 v113, v113
	s_nop 0
	v_mul_f32_e32 v109, v109, v113
	ds_write_b32 v1, v109 offset:18432

.LBB0_2826:
	s_or_b64 exec, exec, s[6:7]
	v_readlane_b32 s4, v255, 6
	s_waitcnt lgkmcnt(0)
	s_barrier
	v_mov_b32_e32 v2, s4
	ds_read_b32 v2, v2
	s_waitcnt lgkmcnt(0)
	v_lshlrev_b32_e32 v7, 8, v2
	v_cmp_lt_i32_e32 vcc, v6, v7
	s_and_saveexec_b64 s[6:7], vcc
	s_cbranch_execz .LBB0_2831
	s_add_u32 s8, s14, 0x49cfe000
	v_readlane_b32 s4, v254, 39
	s_addc_u32 s9, s15, 0
	v_and_b32_e32 v8, 0xff, v6
	s_mov_b32 s11, 0x23000
	v_lshl_add_u32 v9, v6, 2, s4
	v_lshrrev_b32_e32 v10, 8, v6
	v_lshlrev_b32_e32 v10, 4, v10
	v_add_u32_e32 v10, 0x23000, v10
	ds_read2_b32 v[24:25], v10 offset0:128 offset1:130
	ds_read2_b32 v[26:27], v10 offset0:136 offset1:138
	ds_read2_b32 v[28:29], v10 offset0:144 offset1:146
	ds_read2_b32 v[30:31], v10 offset0:152 offset1:154
	ds_read2_b32 v[32:33], v10 offset0:160 offset1:162
	ds_read2_b32 v[34:35], v10 offset0:168 offset1:170
	s_waitcnt lgkmcnt(0)
	v_cmp_lt_i32_e32 vcc, v6, v7
	s_nop 1
	v_cndmask_b32_e32 v48, 0, v25, vcc
	v_cndmask_b32_e32 v24, 0, v24, vcc
	v_cndmask_b32_e64 v54, -1, 0, vcc
	v_lshl_add_u32 v72, v48, 2, s11
	ds_read2_b32 v[36:37], v72 offset1:32
	v_add_u32_e32 v78, 512, v6
	v_cmp_lt_i32_e32 vcc, v78, v7
	s_nop 1
	v_cndmask_b32_e32 v49, 0, v27, vcc
	v_cndmask_b32_e32 v26, 0, v26, vcc
	v_cndmask_b32_e64 v55, -1, 0, vcc
	v_lshl_add_u32 v73, v49, 2, s11
	ds_read2_b32 v[38:39], v73 offset1:32
	v_add_u32_e32 v78, 1024, v6
	v_cmp_lt_i32_e32 vcc, v78, v7
	s_nop 1
	v_cndmask_b32_e32 v50, 0, v29, vcc
	v_cndmask_b32_e32 v28, 0, v28, vcc
	v_cndmask_b32_e64 v56, -1, 0, vcc
	v_lshl_add_u32 v74, v50, 2, s11
	ds_read2_b32 v[40:41], v74 offset1:32
	v_add_u32_e32 v78, 1536, v6
	v_cmp_lt_i32_e32 vcc, v78, v7
	s_nop 1
	v_cndmask_b32_e32 v51, 0, v31, vcc
	v_cndmask_b32_e32 v30, 0, v30, vcc
	v_cndmask_b32_e64 v57, -1, 0, vcc
	v_lshl_add_u32 v75, v51, 2, s11
	ds_read2_b32 v[42:43], v75 offset1:32
	v_add_u32_e32 v78, 2048, v6
	v_cmp_lt_i32_e32 vcc, v78, v7
	s_nop 1
	v_cndmask_b32_e32 v52, 0, v33, vcc
	v_cndmask_b32_e32 v32, 0, v32, vcc
	v_cndmask_b32_e64 v58, -1, 0, vcc
	v_lshl_add_u32 v76, v52, 2, s11
	ds_read2_b32 v[44:45], v76 offset1:32
	v_add_u32_e32 v78, 2560, v6
	v_cmp_lt_i32_e32 vcc, v78, v7
	s_nop 1
	v_cndmask_b32_e32 v53, 0, v35, vcc
	v_cndmask_b32_e32 v34, 0, v34, vcc
	v_cndmask_b32_e64 v59, -1, 0, vcc
	v_lshl_add_u32 v77, v53, 2, s11
	ds_read2_b32 v[46:47], v77 offset1:32
	s_waitcnt lgkmcnt(0)
	v_sub_u32_e32 v60, v24, v37
	v_lshl_or_b32 v60, v60, 8, v8
	v_cmp_lt_i32_e32 vcc, v60, v36
	v_mul_u32_u24_e32 v72, 0x11000, v48
	s_nop 0
	v_cndmask_b32_e32 v60, 0, v60, vcc
	v_cndmask_b32_e64 v79, -1, 0, vcc
	v_or_b32_e32 v54, v54, v79
	v_lshl_add_u32 v60, v60, 2, v72
	global_load_dword v66, v60, s[8:9]
	v_sub_u32_e32 v61, v26, v39
	v_lshl_or_b32 v61, v61, 8, v8
	v_cmp_lt_i32_e32 vcc, v61, v38
	v_mul_u32_u24_e32 v73, 0x11000, v49
	s_nop 0
	v_cndmask_b32_e32 v61, 0, v61, vcc
	v_cndmask_b32_e64 v79, -1, 0, vcc
	v_or_b32_e32 v55, v55, v79
	v_lshl_add_u32 v61, v61, 2, v73
	global_load_dword v67, v61, s[8:9]
	v_sub_u32_e32 v62, v28, v41
	v_lshl_or_b32 v62, v62, 8, v8
	v_cmp_lt_i32_e32 vcc, v62, v40
	v_mul_u32_u24_e32 v74, 0x11000, v50
	s_nop 0
	v_cndmask_b32_e32 v62, 0, v62, vcc
	v_cndmask_b32_e64 v79, -1, 0, vcc
	v_or_b32_e32 v56, v56, v79
	v_lshl_add_u32 v62, v62, 2, v74
	global_load_dword v68, v62, s[8:9]
	v_sub_u32_e32 v63, v30, v43
	v_lshl_or_b32 v63, v63, 8, v8
	v_cmp_lt_i32_e32 vcc, v63, v42
	v_mul_u32_u24_e32 v75, 0x11000, v51
	s_nop 0
	v_cndmask_b32_e32 v63, 0, v63, vcc
	v_cndmask_b32_e64 v79, -1, 0, vcc
	v_or_b32_e32 v57, v57, v79
	v_lshl_add_u32 v63, v63, 2, v75
	global_load_dword v69, v63, s[8:9]
	v_sub_u32_e32 v64, v32, v45
	v_lshl_or_b32 v64, v64, 8, v8
	v_cmp_lt_i32_e32 vcc, v64, v44
	v_mul_u32_u24_e32 v76, 0x11000, v52
	s_nop 0
	v_cndmask_b32_e32 v64, 0, v64, vcc
	v_cndmask_b32_e64 v79, -1, 0, vcc
	v_or_b32_e32 v58, v58, v79
	v_lshl_add_u32 v64, v64, 2, v76
	global_load_dword v70, v64, s[8:9]
	v_sub_u32_e32 v65, v34, v47
	v_lshl_or_b32 v65, v65, 8, v8
	v_cmp_lt_i32_e32 vcc, v65, v46
	v_mul_u32_u24_e32 v77, 0x11000, v53
	s_nop 0
	v_cndmask_b32_e32 v65, 0, v65, vcc
	v_cndmask_b32_e64 v79, -1, 0, vcc
	v_or_b32_e32 v59, v59, v79
	v_lshl_add_u32 v65, v65, 2, v77
	global_load_dword v71, v65, s[8:9]
	s_waitcnt vmcnt(0)
	v_or_b32_e32 v66, v66, v54
	ds_write_b32 v9, v66
	v_or_b32_e32 v67, v67, v55
	ds_write_b32 v9, v67 offset:2048
	v_or_b32_e32 v68, v68, v56
	ds_write_b32 v9, v68 offset:4096
	v_or_b32_e32 v69, v69, v57
	ds_write_b32 v9, v69 offset:6144
	v_or_b32_e32 v70, v70, v58
	ds_write_b32 v9, v70 offset:8192
	v_or_b32_e32 v71, v71, v59
	ds_write_b32 v9, v71 offset:10240
